# baseline (speedup 1.0000x reference)
_Z16sum_layer_kernelPKfS0_Pf:
	s_load_dwordx4 s[4:7], s[0:1], 0x0
	s_load_dwordx2 s[8:9], s[0:1], 0x10
	v_and_b32_e32 v40, 31, v0
	v_bfe_u32 v41, v0, 5, 1
	v_lshrrev_b32_e32 v42, 6, v0
	v_and_b32_e32 v43, 7, v0
	v_bfe_u32 v44, v0, 3, 3
	v_and_b32_e32 v45, 63, v0
	s_lshl_b32 s3, s2, 12
	s_lshl_b32 s19, s2, 7
	v_lshlrev_b32_e32 v1, 11, v41
	v_lshl_or_b32 v1, v40, 2, v1
	v_lshlrev_b32_e32 v46, 4, v43
	v_lshl_add_u32 v35, v44, 16, v46
	v_lshl_add_u32 v35, v42, 21, v35
	v_add_u32_e32 v35, s19, v35
	v_lshlrev_b32_e32 v36, 2, v40
	v_lshl_add_u32 v36, v41, 18, v36
	v_lshl_add_u32 v36, v42, 21, v36
	v_add_u32_e32 v36, s19, v36
	v_mul_u32_u24_e32 v37, 0x1200, v42
	v_mul_u32_u24_e32 v38, 0x90, v44
	v_add3_u32 v38, v37, v38, v46
	v_mul_u32_u24_e32 v39, 0x90, v40
	v_lshlrev_b32_e32 v47, 6, v41
	v_add3_u32 v39, v37, v39, v47
	v_lshrrev_b32_e32 v46, 1, v44
	v_xor_b32_e32 v46, v43, v46
	v_lshlrev_b32_e32 v46, 4, v46
	v_lshl_add_u32 v35, v44, 16, v46
	v_lshl_add_u32 v35, v42, 21, v35
	v_add_u32_e32 v35, s19, v35
	v_xor_b32_e32 v86, 64, v35
	v_readfirstlane_b32 s23, v42
	v_bfe_u32 v47, v40, 1, 3
	v_lshlrev_b32_e32 v39, 2, v41
	v_xor_b32_e32 v39, v39, v47
	s_lshl_b32 s23, s23, 12
	v_lshlrev_b32_e32 v39, 4, v39
	v_lshl_add_u32 v39, v40, 7, v39
	v_lshl_add_u32 v39, v42, 12, v39
	s_mov_b32 m0, s23
	v_xor_b32_e32 v81, 16, v39
	v_xor_b32_e32 v82, 32, v39
	v_xor_b32_e32 v83, 48, v39
	v_cmp_gt_u32_e32 vcc, 32, v45
	v_mov_b32_e32 v34, 0xc1600000
	v_mov_b32_e32 v84, 0x3fb8aa3b
	v_mov_b32_e32 v85, 0x3f317218
	s_mov_b32 s16, 0x3fb8aa3b
	s_mov_b32 s17, 0x3f317218
	s_mov_b32 s20, 0x7fc00
	s_mov_b32 s21, 0xff800
	s_mov_b32 s22, 0x17f400
	s_lshl_b32 s24, 1, 16
	s_lshl_b32 s25, 2, 16
	s_lshl_b32 s26, 3, 16
	s_lshl_b32 s27, 8, 16
	s_lshl_b32 s28, 9, 16
	s_lshl_b32 s29, 10, 16
	s_lshl_b32 s30, 11, 16
	s_lshl_b32 s31, 16, 16
	s_lshl_b32 s32, 17, 16
	s_lshl_b32 s33, 18, 16
	s_lshl_b32 s34, 19, 16
	s_lshl_b32 s35, 24, 16
	s_lshl_b32 s36, 25, 16
	s_lshl_b32 s37, 26, 16
	s_lshl_b32 s38, 27, 16
	s_mov_b32 s14, 0x200000
	s_mov_b32 s15, 0x20000
	s_waitcnt lgkmcnt(0)
	s_mov_b32 s12, s6
	s_and_b32 s13, s7, 0xffff
	s_and_b32 s5, s5, 0xffff
	s_mov_b32 s6, 0x800000
	s_mov_b32 s7, s15
	s_and_b32 s9, s9, 0xffff
	s_mov_b32 s10, s6
	s_mov_b32 s11, s15
	buffer_load_dword v18, v1, s[12:15], s3 offen nt
	buffer_load_dword v19, v1, s[12:15], s3 offen offset:128 nt
	buffer_load_dword v20, v1, s[12:15], s3 offen offset:256 nt
	buffer_load_dword v21, v1, s[12:15], s3 offen offset:384 nt
	buffer_load_dword v22, v1, s[12:15], s3 offen offset:512 nt
	buffer_load_dword v23, v1, s[12:15], s3 offen offset:640 nt
	buffer_load_dword v24, v1, s[12:15], s3 offen offset:768 nt
	buffer_load_dword v25, v1, s[12:15], s3 offen offset:896 nt
	buffer_load_dword v26, v1, s[12:15], s3 offen offset:1024 nt
	buffer_load_dword v27, v1, s[12:15], s3 offen offset:1152 nt
	buffer_load_dword v28, v1, s[12:15], s3 offen offset:1280 nt
	buffer_load_dword v29, v1, s[12:15], s3 offen offset:1408 nt
	buffer_load_dword v30, v1, s[12:15], s3 offen offset:1536 nt
	buffer_load_dword v31, v1, s[12:15], s3 offen offset:1664 nt
	buffer_load_dword v32, v1, s[12:15], s3 offen offset:1792 nt
	buffer_load_dword v33, v1, s[12:15], s3 offen offset:1920 nt
	buffer_load_dwordx4 v35, s[4:7], 0 offen nt lds
	buffer_load_dwordx4 v86, s[4:7], s20 offen offset:1024 nt lds
	buffer_load_dwordx4 v35, s[4:7], s21 offen offset:2048 nt lds
	buffer_load_dwordx4 v86, s[4:7], s22 offen offset:3072 nt lds
	s_waitcnt vmcnt(17)
	v_max3_f32 v48, v18, v19, v20
	s_waitcnt vmcnt(14)
	v_max3_f32 v50, v21, v22, v23
	s_waitcnt vmcnt(12)
	v_max3_f32 v48, v48, v24, v25
	s_waitcnt vmcnt(10)
	v_max3_f32 v50, v50, v26, v27
	s_waitcnt vmcnt(8)
	v_max3_f32 v48, v48, v28, v29
	s_waitcnt vmcnt(6)
	v_max3_f32 v50, v50, v30, v31
	s_waitcnt vmcnt(4)
	v_max3_f32 v48, v48, v32, v33
	v_max_f32_e32 v48, v48, v50
	v_mov_b32_e32 v50, v48
	s_nop 1
	v_permlane32_swap_b32_e32 v48, v50
	v_max_f32_e32 v48, v48, v50
	v_fmamk_f32 v48, v48, 0x3fb8aa3b, v34
	v_pk_fma_f32 v[18:19], v[18:19], v[84:85], v[48:49] op_sel_hi:[1,0,0] neg_lo:[0,0,1] neg_hi:[0,0,1]
	v_exp_f32_e32 v18, v18
	v_exp_f32_e32 v19, v19
	v_pk_fma_f32 v[20:21], v[20:21], v[84:85], v[48:49] op_sel_hi:[1,0,0] neg_lo:[0,0,1] neg_hi:[0,0,1]
	v_exp_f32_e32 v20, v20
	v_exp_f32_e32 v21, v21
	v_pk_fma_f32 v[22:23], v[22:23], v[84:85], v[48:49] op_sel_hi:[1,0,0] neg_lo:[0,0,1] neg_hi:[0,0,1]
	v_exp_f32_e32 v22, v22
	v_exp_f32_e32 v23, v23
	v_pk_fma_f32 v[24:25], v[24:25], v[84:85], v[48:49] op_sel_hi:[1,0,0] neg_lo:[0,0,1] neg_hi:[0,0,1]
	v_exp_f32_e32 v24, v24
	v_exp_f32_e32 v25, v25
	v_pk_fma_f32 v[26:27], v[26:27], v[84:85], v[48:49] op_sel_hi:[1,0,0] neg_lo:[0,0,1] neg_hi:[0,0,1]
	v_exp_f32_e32 v26, v26
	v_exp_f32_e32 v27, v27
	v_pk_fma_f32 v[28:29], v[28:29], v[84:85], v[48:49] op_sel_hi:[1,0,0] neg_lo:[0,0,1] neg_hi:[0,0,1]
	v_exp_f32_e32 v28, v28
	v_exp_f32_e32 v29, v29
	v_pk_fma_f32 v[30:31], v[30:31], v[84:85], v[48:49] op_sel_hi:[1,0,0] neg_lo:[0,0,1] neg_hi:[0,0,1]
	v_exp_f32_e32 v30, v30
	v_exp_f32_e32 v31, v31
	v_pk_fma_f32 v[32:33], v[32:33], v[84:85], v[48:49] op_sel_hi:[1,0,0] neg_lo:[0,0,1] neg_hi:[0,0,1]
	v_exp_f32_e32 v32, v32
	v_exp_f32_e32 v33, v33
	v_pk_add_f32 v[56:57], v[18:19], v[20:21]
	v_pk_add_f32 v[58:59], v[22:23], v[24:25]
	v_pk_add_f32 v[60:61], v[26:27], v[28:29]
	v_pk_add_f32 v[62:63], v[30:31], v[32:33]
	v_pk_add_f32 v[56:57], v[56:57], v[58:59]
	v_pk_add_f32 v[60:61], v[60:61], v[62:63]
	v_pk_add_f32 v[56:57], v[56:57], v[60:61]
	v_add_f32_e32 v50, v56, v57
	v_mov_b32_e32 v51, v50
	s_nop 1
	v_permlane32_swap_b32_e32 v50, v51
	v_add_f32_e32 v50, v50, v51
	v_log_f32_e32 v50, v50
	v_cvt_pk_f16_f32 v40, v18, v19
	v_cvt_pk_f16_f32 v41, v20, v21
	v_cvt_pk_f16_f32 v42, v22, v23
	v_cvt_pk_f16_f32 v43, v24, v25
	v_cvt_pk_f16_f32 v44, v26, v27
	v_cvt_pk_f16_f32 v45, v28, v29
	v_cvt_pk_f16_f32 v46, v30, v31
	v_cvt_pk_f16_f32 v47, v32, v33
	v_add_f32_e32 v50, 0x41600000, v50
	v_mul_f32_e32 v50, 0xbf317218, v50
	v_cndmask_b32_e64 v51, v50, 1.0, vcc
	s_waitcnt vmcnt(0)
	ds_read_b128 v[2:5], v39
	ds_read_b128 v[6:9], v81
	ds_read_b128 v[10:13], v82
	ds_read_b128 v[14:17], v83
	s_waitcnt lgkmcnt(2)
	v_max3_f32 v52, v2, v3, v4
	v_max3_f32 v53, v5, v6, v7
	v_max_f32_e32 v52, v52, v8
	v_max_f32_e32 v53, v53, v9
	s_waitcnt lgkmcnt(0)
	v_max3_f32 v52, v52, v10, v11
	v_max3_f32 v53, v53, v12, v13
	v_max3_f32 v52, v52, v14, v15
	v_max3_f32 v53, v53, v16, v17
	v_max_f32_e32 v52, v52, v53
	v_mov_b32_e32 v53, v52
	s_nop 1
	v_permlane32_swap_b32_e32 v52, v53
	v_max_f32_e32 v52, v52, v53
	v_cndmask_b32_e32 v54, 1.0, v52, vcc
	v_fmamk_f32 v48, v52, 0x3fb8aa3b, v34
	v_pk_fma_f32 v[2:3], v[2:3], v[84:85], v[48:49] op_sel_hi:[1,0,0] neg_lo:[0,0,1] neg_hi:[0,0,1]
	v_mfma_f32_32x32x2_f32 v[64:79], v54, v51, 0
	v_exp_f32_e32 v2, v2
	v_exp_f32_e32 v3, v3
	v_pk_fma_f32 v[4:5], v[4:5], v[84:85], v[48:49] op_sel_hi:[1,0,0] neg_lo:[0,0,1] neg_hi:[0,0,1]
	v_exp_f32_e32 v4, v4
	v_exp_f32_e32 v5, v5
	v_pk_fma_f32 v[6:7], v[6:7], v[84:85], v[48:49] op_sel_hi:[1,0,0] neg_lo:[0,0,1] neg_hi:[0,0,1]
	v_exp_f32_e32 v6, v6
	v_exp_f32_e32 v7, v7
	v_pk_fma_f32 v[8:9], v[8:9], v[84:85], v[48:49] op_sel_hi:[1,0,0] neg_lo:[0,0,1] neg_hi:[0,0,1]
	v_exp_f32_e32 v8, v8
	v_exp_f32_e32 v9, v9
	v_pk_fma_f32 v[10:11], v[10:11], v[84:85], v[48:49] op_sel_hi:[1,0,0] neg_lo:[0,0,1] neg_hi:[0,0,1]
	v_exp_f32_e32 v10, v10
	v_cvt_pk_f16_f32 v56, v2, v3
	v_cvt_pk_f16_f32 v57, v4, v5
	v_cvt_pk_f16_f32 v58, v6, v7
	v_cvt_pk_f16_f32 v59, v8, v9
	v_exp_f32_e32 v11, v11
	v_pk_fma_f32 v[12:13], v[12:13], v[84:85], v[48:49] op_sel_hi:[1,0,0] neg_lo:[0,0,1] neg_hi:[0,0,1]
	v_exp_f32_e32 v12, v12
	v_mfma_f32_32x32x16_f16 v[18:33], v[56:59], v[40:43], 0
	v_exp_f32_e32 v13, v13
	v_pk_fma_f32 v[14:15], v[14:15], v[84:85], v[48:49] op_sel_hi:[1,0,0] neg_lo:[0,0,1] neg_hi:[0,0,1]
	v_exp_f32_e32 v14, v14
	v_exp_f32_e32 v15, v15
	v_pk_fma_f32 v[16:17], v[16:17], v[84:85], v[48:49] op_sel_hi:[1,0,0] neg_lo:[0,0,1] neg_hi:[0,0,1]
	v_exp_f32_e32 v16, v16
	v_exp_f32_e32 v17, v17
	v_cvt_pk_f16_f32 v60, v10, v11
	v_cvt_pk_f16_f32 v61, v12, v13
	v_cvt_pk_f16_f32 v62, v14, v15
	v_cvt_pk_f16_f32 v63, v16, v17
	s_nop 1
	v_mfma_f32_32x32x16_f16 v[18:33], v[60:63], v[44:47], v[18:33]
	s_nop 11
	v_log_f32_e32 v18, v18
	v_log_f32_e32 v19, v19
	v_log_f32_e32 v20, v20
	v_log_f32_e32 v21, v21
	v_log_f32_e32 v22, v22
	v_log_f32_e32 v23, v23
	v_pk_fma_f32 v[64:65], v[18:19], v[84:85], v[64:65] op_sel:[0,1,0] op_sel_hi:[1,1,1]
	buffer_store_dword v64, v36, s[8:11], 0 offen
	buffer_store_dword v65, v36, s[8:11], s24 offen
	v_log_f32_e32 v24, v24
	v_log_f32_e32 v25, v25
	v_pk_fma_f32 v[66:67], v[20:21], v[84:85], v[66:67] op_sel:[0,1,0] op_sel_hi:[1,1,1]
	buffer_store_dword v66, v36, s[8:11], s25 offen
	buffer_store_dword v67, v36, s[8:11], s26 offen
	v_log_f32_e32 v26, v26
	v_log_f32_e32 v27, v27
	v_pk_fma_f32 v[68:69], v[22:23], v[84:85], v[68:69] op_sel:[0,1,0] op_sel_hi:[1,1,1]
	buffer_store_dword v68, v36, s[8:11], s27 offen
	buffer_store_dword v69, v36, s[8:11], s28 offen
	v_log_f32_e32 v28, v28
	v_log_f32_e32 v29, v29
	v_pk_fma_f32 v[70:71], v[24:25], v[84:85], v[70:71] op_sel:[0,1,0] op_sel_hi:[1,1,1]
	buffer_store_dword v70, v36, s[8:11], s29 offen
	buffer_store_dword v71, v36, s[8:11], s30 offen
	v_log_f32_e32 v30, v30
	v_log_f32_e32 v31, v31
	v_pk_fma_f32 v[72:73], v[26:27], v[84:85], v[72:73] op_sel:[0,1,0] op_sel_hi:[1,1,1]
	buffer_store_dword v72, v36, s[8:11], s31 offen
	buffer_store_dword v73, v36, s[8:11], s32 offen
	v_log_f32_e32 v32, v32
	v_log_f32_e32 v33, v33
	v_pk_fma_f32 v[74:75], v[28:29], v[84:85], v[74:75] op_sel:[0,1,0] op_sel_hi:[1,1,1]
	buffer_store_dword v74, v36, s[8:11], s33 offen
	buffer_store_dword v75, v36, s[8:11], s34 offen
	v_pk_fma_f32 v[76:77], v[30:31], v[84:85], v[76:77] op_sel:[0,1,0] op_sel_hi:[1,1,1]
	buffer_store_dword v76, v36, s[8:11], s35 offen
	buffer_store_dword v77, v36, s[8:11], s36 offen
	v_pk_fma_f32 v[78:79], v[32:33], v[84:85], v[78:79] op_sel:[0,1,0] op_sel_hi:[1,1,1]
	buffer_store_dword v78, v36, s[8:11], s37 offen
	buffer_store_dword v79, v36, s[8:11], s38 offen
	s_endpgm
